# ordered-emission per-key core shortened to 10 instructions (running write position and remaining-tie counter instead of two counters and three mask ops); plus predicated level-2 histogram pass
# speedup vs baseline: 1.0189x; 1.0033x over previous
.LBB0_718:
	v_lshl_add_u64 v[8:9], v[6:7], 1, s[12:13]
	global_load_dwordx4 v[4:7], v[8:9], off offset:16
	s_nop 0
	global_load_dwordx4 v[8:11], v[8:9], off
	s_and_saveexec_b64 s[24:25], vcc
	s_cbranch_execz .LBB0_845
	ds_read_u16 v2, v49 offset:36864
	v_add_u32_e32 v44, 0x11200, v49
	ds_read_b32 v44, v44
	s_waitcnt vmcnt(6)
	s_waitcnt lgkmcnt(1)
	v_lshrrev_b32_e32 v45, 8, v2
	v_and_b32_e32 v2, 0xff, v2
	v_cndmask_b32_e64 v45, v45, 0, s[22:23]
	v_cndmask_b32_e64 v2, v2, 0, s[22:23]
	s_waitcnt lgkmcnt(0)
	v_add_u32_sdwa v51, v45, v44 dst_sel:DWORD dst_unused:UNUSED_PAD src0_sel:DWORD src1_sel:WORD_1
	v_add_u32_sdwa v214, v2, v44 dst_sel:DWORD dst_unused:UNUSED_PAD src0_sel:DWORD src1_sel:WORD_0
	v_lshl_add_u64 v[44:45], v[40:41], 0, s[16:17]
	v_min_i32_e32 v2, v51, v37
	v_add_u32_e32 v2, v2, v214
	v_sub_u32_e32 v51, v37, v51
	v_med3_i32 v214, v51, 0, 1
	v_sub_u32_e32 v214, v36, v214
	v_cmp_gt_i32_sdwa s[0:1], v32, v214 src0_sel:WORD_0 src1_sel:DWORD
	v_cmp_eq_u32_sdwa s[30:31], v32, v36 src0_sel:WORD_0 src1_sel:DWORD
	v_lshl_add_u64 v[46:47], v[2:3], 1, v[38:39]
	s_and_saveexec_b64 s[34:35], s[0:1]
	global_store_short v[46:47], v44, off
	s_mov_b64 exec, s[34:35]
	v_addc_co_u32_e64 v2, vcc, 0, v2, s[0:1]
	v_subb_co_u32_e64 v51, vcc, v51, 0, s[30:31]
	v_lshl_add_u64 v[46:47], v[44:45], 0, 1
	v_med3_i32 v214, v51, 0, 1
	v_sub_u32_e32 v214, v36, v214
	v_cmp_gt_i32_sdwa s[0:1], v32, v214 src0_sel:WORD_1 src1_sel:DWORD
	v_cmp_eq_u32_sdwa s[30:31], v32, v36 src0_sel:WORD_1 src1_sel:DWORD
	v_lshl_add_u64 v[212:213], v[2:3], 1, v[38:39]
	s_and_saveexec_b64 s[34:35], s[0:1]
	global_store_short v[212:213], v46, off
	s_mov_b64 exec, s[34:35]
	v_addc_co_u32_e64 v2, vcc, 0, v2, s[0:1]
	v_subb_co_u32_e64 v51, vcc, v51, 0, s[30:31]
	v_lshl_add_u64 v[46:47], v[44:45], 0, 2
	v_med3_i32 v214, v51, 0, 1
	v_sub_u32_e32 v214, v36, v214
	v_cmp_gt_i32_sdwa s[0:1], v33, v214 src0_sel:WORD_0 src1_sel:DWORD
	v_cmp_eq_u32_sdwa s[30:31], v33, v36 src0_sel:WORD_0 src1_sel:DWORD
	v_lshl_add_u64 v[212:213], v[2:3], 1, v[38:39]
	s_and_saveexec_b64 s[34:35], s[0:1]
	global_store_short v[212:213], v46, off
	s_mov_b64 exec, s[34:35]
	v_addc_co_u32_e64 v2, vcc, 0, v2, s[0:1]
	v_subb_co_u32_e64 v51, vcc, v51, 0, s[30:31]
	v_lshl_add_u64 v[46:47], v[44:45], 0, 3
	v_med3_i32 v214, v51, 0, 1
	v_sub_u32_e32 v214, v36, v214
	v_cmp_gt_i32_sdwa s[0:1], v33, v214 src0_sel:WORD_1 src1_sel:DWORD
	v_cmp_eq_u32_sdwa s[30:31], v33, v36 src0_sel:WORD_1 src1_sel:DWORD
	v_lshl_add_u64 v[32:33], v[2:3], 1, v[38:39]
	s_and_saveexec_b64 s[34:35], s[0:1]
	global_store_short v[32:33], v46, off
	s_mov_b64 exec, s[34:35]
	v_addc_co_u32_e64 v2, vcc, 0, v2, s[0:1]
	v_subb_co_u32_e64 v51, vcc, v51, 0, s[30:31]
	v_lshl_add_u64 v[32:33], v[44:45], 0, 4
	v_med3_i32 v214, v51, 0, 1
	v_sub_u32_e32 v214, v36, v214
	v_cmp_gt_i32_sdwa s[0:1], v34, v214 src0_sel:WORD_0 src1_sel:DWORD
	v_cmp_eq_u32_sdwa s[30:31], v34, v36 src0_sel:WORD_0 src1_sel:DWORD
	v_lshl_add_u64 v[46:47], v[2:3], 1, v[38:39]
	s_and_saveexec_b64 s[34:35], s[0:1]
	global_store_short v[46:47], v32, off
	s_mov_b64 exec, s[34:35]
	v_addc_co_u32_e64 v2, vcc, 0, v2, s[0:1]
	v_subb_co_u32_e64 v51, vcc, v51, 0, s[30:31]
	v_lshl_add_u64 v[32:33], v[44:45], 0, 5
	v_med3_i32 v214, v51, 0, 1
	v_sub_u32_e32 v214, v36, v214
	v_cmp_gt_i32_sdwa s[0:1], v34, v214 src0_sel:WORD_1 src1_sel:DWORD
	v_cmp_eq_u32_sdwa s[30:31], v34, v36 src0_sel:WORD_1 src1_sel:DWORD
	v_lshl_add_u64 v[46:47], v[2:3], 1, v[38:39]
	s_and_saveexec_b64 s[34:35], s[0:1]
	global_store_short v[46:47], v32, off
	s_mov_b64 exec, s[34:35]
	v_addc_co_u32_e64 v2, vcc, 0, v2, s[0:1]
	v_subb_co_u32_e64 v51, vcc, v51, 0, s[30:31]
	v_lshl_add_u64 v[32:33], v[44:45], 0, 6
	v_med3_i32 v214, v51, 0, 1
	v_sub_u32_e32 v214, v36, v214
	v_cmp_gt_i32_sdwa s[0:1], v35, v214 src0_sel:WORD_0 src1_sel:DWORD
	v_cmp_eq_u32_sdwa s[30:31], v35, v36 src0_sel:WORD_0 src1_sel:DWORD
	v_lshl_add_u64 v[46:47], v[2:3], 1, v[38:39]
	s_and_saveexec_b64 s[34:35], s[0:1]
	global_store_short v[46:47], v32, off
	s_mov_b64 exec, s[34:35]
	v_addc_co_u32_e64 v2, vcc, 0, v2, s[0:1]
	v_subb_co_u32_e64 v51, vcc, v51, 0, s[30:31]
	v_lshl_add_u64 v[32:33], v[44:45], 0, 7
	v_med3_i32 v214, v51, 0, 1
	v_sub_u32_e32 v214, v36, v214
	v_cmp_gt_i32_sdwa s[0:1], v35, v214 src0_sel:WORD_1 src1_sel:DWORD
	v_cmp_eq_u32_sdwa s[30:31], v35, v36 src0_sel:WORD_1 src1_sel:DWORD
	v_lshl_add_u64 v[34:35], v[2:3], 1, v[38:39]
	s_and_saveexec_b64 s[34:35], s[0:1]
	global_store_short v[34:35], v32, off
	s_mov_b64 exec, s[34:35]
	v_addc_co_u32_e64 v2, vcc, 0, v2, s[0:1]
	v_subb_co_u32_e64 v51, vcc, v51, 0, s[30:31]
	v_lshl_add_u64 v[32:33], v[44:45], 0, 8
	v_med3_i32 v214, v51, 0, 1
	v_sub_u32_e32 v214, v36, v214
	v_cmp_gt_i32_sdwa s[0:1], v28, v214 src0_sel:WORD_0 src1_sel:DWORD
	v_cmp_eq_u32_sdwa s[30:31], v28, v36 src0_sel:WORD_0 src1_sel:DWORD
	v_lshl_add_u64 v[34:35], v[2:3], 1, v[38:39]
	s_and_saveexec_b64 s[34:35], s[0:1]
	global_store_short v[34:35], v32, off
	s_mov_b64 exec, s[34:35]
	v_addc_co_u32_e64 v2, vcc, 0, v2, s[0:1]
	v_subb_co_u32_e64 v51, vcc, v51, 0, s[30:31]
	v_lshl_add_u64 v[32:33], v[44:45], 0, 9
	v_med3_i32 v214, v51, 0, 1
	v_sub_u32_e32 v214, v36, v214
	v_cmp_gt_i32_sdwa s[0:1], v28, v214 src0_sel:WORD_1 src1_sel:DWORD
	v_cmp_eq_u32_sdwa s[30:31], v28, v36 src0_sel:WORD_1 src1_sel:DWORD
	v_lshl_add_u64 v[34:35], v[2:3], 1, v[38:39]
	s_and_saveexec_b64 s[34:35], s[0:1]
	global_store_short v[34:35], v32, off
	s_mov_b64 exec, s[34:35]
	v_addc_co_u32_e64 v2, vcc, 0, v2, s[0:1]
	v_subb_co_u32_e64 v51, vcc, v51, 0, s[30:31]
	v_lshl_add_u64 v[32:33], v[44:45], 0, 10
	v_med3_i32 v214, v51, 0, 1
	v_sub_u32_e32 v214, v36, v214
	v_cmp_gt_i32_sdwa s[0:1], v29, v214 src0_sel:WORD_0 src1_sel:DWORD
	v_cmp_eq_u32_sdwa s[30:31], v29, v36 src0_sel:WORD_0 src1_sel:DWORD
	v_lshl_add_u64 v[34:35], v[2:3], 1, v[38:39]
	s_and_saveexec_b64 s[34:35], s[0:1]
	global_store_short v[34:35], v32, off
	s_mov_b64 exec, s[34:35]
	v_addc_co_u32_e64 v2, vcc, 0, v2, s[0:1]
	v_subb_co_u32_e64 v51, vcc, v51, 0, s[30:31]
	v_lshl_add_u64 v[32:33], v[44:45], 0, 11
	v_med3_i32 v214, v51, 0, 1
	v_sub_u32_e32 v214, v36, v214
	v_cmp_gt_i32_sdwa s[0:1], v29, v214 src0_sel:WORD_1 src1_sel:DWORD
	v_cmp_eq_u32_sdwa s[30:31], v29, v36 src0_sel:WORD_1 src1_sel:DWORD
	v_lshl_add_u64 v[28:29], v[2:3], 1, v[38:39]
	s_and_saveexec_b64 s[34:35], s[0:1]
	global_store_short v[28:29], v32, off
	s_mov_b64 exec, s[34:35]
	v_addc_co_u32_e64 v2, vcc, 0, v2, s[0:1]
	v_subb_co_u32_e64 v51, vcc, v51, 0, s[30:31]
	v_lshl_add_u64 v[28:29], v[44:45], 0, 12
	v_med3_i32 v214, v51, 0, 1
	v_sub_u32_e32 v214, v36, v214
	v_cmp_gt_i32_sdwa s[0:1], v30, v214 src0_sel:WORD_0 src1_sel:DWORD
	v_cmp_eq_u32_sdwa s[30:31], v30, v36 src0_sel:WORD_0 src1_sel:DWORD
	v_lshl_add_u64 v[32:33], v[2:3], 1, v[38:39]
	s_and_saveexec_b64 s[34:35], s[0:1]
	global_store_short v[32:33], v28, off
	s_mov_b64 exec, s[34:35]
	v_addc_co_u32_e64 v2, vcc, 0, v2, s[0:1]
	v_subb_co_u32_e64 v51, vcc, v51, 0, s[30:31]
	v_lshl_add_u64 v[28:29], v[44:45], 0, 13
	v_med3_i32 v214, v51, 0, 1
	v_sub_u32_e32 v214, v36, v214
	v_cmp_gt_i32_sdwa s[0:1], v30, v214 src0_sel:WORD_1 src1_sel:DWORD
	v_cmp_eq_u32_sdwa s[30:31], v30, v36 src0_sel:WORD_1 src1_sel:DWORD
	v_lshl_add_u64 v[32:33], v[2:3], 1, v[38:39]
	s_and_saveexec_b64 s[34:35], s[0:1]
	global_store_short v[32:33], v28, off
	s_mov_b64 exec, s[34:35]
	v_addc_co_u32_e64 v2, vcc, 0, v2, s[0:1]
	v_subb_co_u32_e64 v51, vcc, v51, 0, s[30:31]
	v_lshl_add_u64 v[28:29], v[44:45], 0, 14
	v_med3_i32 v214, v51, 0, 1
	v_sub_u32_e32 v214, v36, v214
	v_cmp_gt_i32_sdwa s[0:1], v31, v214 src0_sel:WORD_0 src1_sel:DWORD
	v_cmp_eq_u32_sdwa s[30:31], v31, v36 src0_sel:WORD_0 src1_sel:DWORD
	v_lshl_add_u64 v[32:33], v[2:3], 1, v[38:39]
	s_and_saveexec_b64 s[34:35], s[0:1]
	global_store_short v[32:33], v28, off
	s_mov_b64 exec, s[34:35]
	v_addc_co_u32_e64 v2, vcc, 0, v2, s[0:1]
	v_subb_co_u32_e64 v51, vcc, v51, 0, s[30:31]
	v_sub_u32_e32 v51, v37, v51
	v_min_i32_e32 v214, v51, v37
	v_sub_u32_e32 v214, v2, v214
	v_cmp_le_u32_sdwa s[30:31], v31, v36 src0_sel:WORD_1 src1_sel:DWORD
	s_mov_b64 s[0:1], 0
	s_and_saveexec_b64 s[34:35], s[30:31]
	s_xor_b64 s[30:31], exec, s[34:35]
	s_cbranch_execz .LBB0_1230
	v_cmp_eq_u32_sdwa s[0:1], v31, v36 src0_sel:WORD_1 src1_sel:DWORD
	v_cmp_lt_i32_e32 vcc, v51, v37
	s_and_b64 s[38:39], s[0:1], vcc
	s_mov_b64 s[0:1], 0
	s_and_saveexec_b64 s[34:35], s[38:39]
	v_add_u32_e32 v2, v51, v214
	s_mov_b64 s[0:1], exec
	v_mov_b64_e32 v[28:29], v[2:3]
	s_or_b64 exec, exec, s[34:35]
	s_and_b64 s[0:1], s[0:1], exec
	s_andn2_saveexec_b64 s[30:31], s[30:31]
	s_cbranch_execnz .LBB0_1231

.LBB0_845:
	s_or_b64 exec, exec, s[24:25]
	s_andn2_b64 vcc, exec, s[18:19]
	s_cbranch_vccnz .LBB0_975
	ds_read_u16 v2, v50 offset:36896
	s_waitcnt lgkmcnt(0)
	v_cmp_ne_u16_e32 vcc, 0, v2
	s_and_saveexec_b64 s[18:19], vcc
	s_cbranch_execz .LBB0_973
	ds_read_u16 v2, v49 offset:36896
	s_waitcnt vmcnt(7)
	v_add_u32_e32 v28, 0x11220, v49
	ds_read_b32 v28, v28
	v_lshl_add_u64 v[30:31], v[40:41], 0, s[16:17]
	s_waitcnt vmcnt(4)
	s_waitcnt lgkmcnt(1)
	v_lshrrev_b32_e32 v29, 8, v2
	v_and_b32_e32 v2, 0xff, v2
	v_cndmask_b32_e64 v29, v29, 0, s[22:23]
	v_cndmask_b32_e64 v2, v2, 0, s[22:23]
	s_waitcnt lgkmcnt(0)
	v_add_u32_sdwa v34, v29, v28 dst_sel:DWORD dst_unused:UNUSED_PAD src0_sel:DWORD src1_sel:WORD_1
	v_add_u32_sdwa v35, v2, v28 dst_sel:DWORD dst_unused:UNUSED_PAD src0_sel:DWORD src1_sel:WORD_0
	v_lshl_add_u64 v[28:29], v[30:31], 0, s[84:85]
	v_min_i32_e32 v2, v34, v37
	v_add_u32_e32 v2, v2, v35
	v_sub_u32_e32 v34, v37, v34
	v_med3_i32 v35, v34, 0, 1
	v_sub_u32_e32 v35, v36, v35
	v_cmp_gt_i32_sdwa s[0:1], v24, v35 src0_sel:WORD_0 src1_sel:DWORD
	v_cmp_eq_u32_sdwa s[24:25], v24, v36 src0_sel:WORD_0 src1_sel:DWORD
	v_lshl_add_u64 v[32:33], v[2:3], 1, v[38:39]
	s_and_saveexec_b64 s[30:31], s[0:1]
	global_store_short v[32:33], v28, off
	s_mov_b64 exec, s[30:31]
	v_addc_co_u32_e64 v2, vcc, 0, v2, s[0:1]
	v_subb_co_u32_e64 v34, vcc, v34, 0, s[24:25]
	s_mov_b64 s[0:1], 0x101
	v_lshl_add_u64 v[32:33], v[30:31], 0, s[0:1]
	v_med3_i32 v35, v34, 0, 1
	v_sub_u32_e32 v35, v36, v35
	v_cmp_gt_i32_sdwa s[0:1], v24, v35 src0_sel:WORD_1 src1_sel:DWORD
	v_cmp_eq_u32_sdwa s[24:25], v24, v36 src0_sel:WORD_1 src1_sel:DWORD
	v_lshl_add_u64 v[44:45], v[2:3], 1, v[38:39]
	s_and_saveexec_b64 s[30:31], s[0:1]
	global_store_short v[44:45], v32, off
	s_mov_b64 exec, s[30:31]
	v_addc_co_u32_e64 v2, vcc, 0, v2, s[0:1]
	v_subb_co_u32_e64 v34, vcc, v34, 0, s[24:25]
	s_mov_b64 s[0:1], 0x102
	v_lshl_add_u64 v[32:33], v[30:31], 0, s[0:1]
	v_med3_i32 v35, v34, 0, 1
	v_sub_u32_e32 v35, v36, v35
	v_cmp_gt_i32_sdwa s[0:1], v25, v35 src0_sel:WORD_0 src1_sel:DWORD
	v_cmp_eq_u32_sdwa s[24:25], v25, v36 src0_sel:WORD_0 src1_sel:DWORD
	v_lshl_add_u64 v[44:45], v[2:3], 1, v[38:39]
	s_and_saveexec_b64 s[30:31], s[0:1]
	global_store_short v[44:45], v32, off
	s_mov_b64 exec, s[30:31]
	v_addc_co_u32_e64 v2, vcc, 0, v2, s[0:1]
	v_subb_co_u32_e64 v34, vcc, v34, 0, s[24:25]
	s_mov_b64 s[0:1], 0x103
	v_lshl_add_u64 v[32:33], v[30:31], 0, s[0:1]
	v_med3_i32 v35, v34, 0, 1
	v_sub_u32_e32 v35, v36, v35
	v_cmp_gt_i32_sdwa s[0:1], v25, v35 src0_sel:WORD_1 src1_sel:DWORD
	v_cmp_eq_u32_sdwa s[24:25], v25, v36 src0_sel:WORD_1 src1_sel:DWORD
	v_lshl_add_u64 v[24:25], v[2:3], 1, v[38:39]
	s_and_saveexec_b64 s[30:31], s[0:1]
	global_store_short v[24:25], v32, off
	s_mov_b64 exec, s[30:31]
	v_addc_co_u32_e64 v2, vcc, 0, v2, s[0:1]
	v_subb_co_u32_e64 v34, vcc, v34, 0, s[24:25]
	s_mov_b64 s[0:1], 0x104
	v_lshl_add_u64 v[24:25], v[30:31], 0, s[0:1]
	v_med3_i32 v35, v34, 0, 1
	v_sub_u32_e32 v35, v36, v35
	v_cmp_gt_i32_sdwa s[0:1], v26, v35 src0_sel:WORD_0 src1_sel:DWORD
	v_cmp_eq_u32_sdwa s[24:25], v26, v36 src0_sel:WORD_0 src1_sel:DWORD
	v_lshl_add_u64 v[32:33], v[2:3], 1, v[38:39]
	s_and_saveexec_b64 s[30:31], s[0:1]
	global_store_short v[32:33], v24, off
	s_mov_b64 exec, s[30:31]
	v_addc_co_u32_e64 v2, vcc, 0, v2, s[0:1]
	v_subb_co_u32_e64 v34, vcc, v34, 0, s[24:25]
	s_mov_b64 s[0:1], 0x105
	v_lshl_add_u64 v[24:25], v[30:31], 0, s[0:1]
	v_med3_i32 v35, v34, 0, 1
	v_sub_u32_e32 v35, v36, v35
	v_cmp_gt_i32_sdwa s[0:1], v26, v35 src0_sel:WORD_1 src1_sel:DWORD
	v_cmp_eq_u32_sdwa s[24:25], v26, v36 src0_sel:WORD_1 src1_sel:DWORD
	v_lshl_add_u64 v[32:33], v[2:3], 1, v[38:39]
	s_and_saveexec_b64 s[30:31], s[0:1]
	global_store_short v[32:33], v24, off
	s_mov_b64 exec, s[30:31]
	v_addc_co_u32_e64 v2, vcc, 0, v2, s[0:1]
	v_subb_co_u32_e64 v34, vcc, v34, 0, s[24:25]
	s_mov_b64 s[0:1], 0x106
	v_lshl_add_u64 v[24:25], v[30:31], 0, s[0:1]
	v_med3_i32 v35, v34, 0, 1
	v_sub_u32_e32 v35, v36, v35
	v_cmp_gt_i32_sdwa s[0:1], v27, v35 src0_sel:WORD_0 src1_sel:DWORD
	v_cmp_eq_u32_sdwa s[24:25], v27, v36 src0_sel:WORD_0 src1_sel:DWORD
	v_lshl_add_u64 v[32:33], v[2:3], 1, v[38:39]
	s_and_saveexec_b64 s[30:31], s[0:1]
	global_store_short v[32:33], v24, off
	s_mov_b64 exec, s[30:31]
	v_addc_co_u32_e64 v2, vcc, 0, v2, s[0:1]
	v_subb_co_u32_e64 v34, vcc, v34, 0, s[24:25]
	s_mov_b64 s[0:1], 0x107
	v_lshl_add_u64 v[24:25], v[30:31], 0, s[0:1]
	v_med3_i32 v35, v34, 0, 1
	v_sub_u32_e32 v35, v36, v35
	v_cmp_gt_i32_sdwa s[0:1], v27, v35 src0_sel:WORD_1 src1_sel:DWORD
	v_cmp_eq_u32_sdwa s[24:25], v27, v36 src0_sel:WORD_1 src1_sel:DWORD
	v_lshl_add_u64 v[26:27], v[2:3], 1, v[38:39]
	s_and_saveexec_b64 s[30:31], s[0:1]
	global_store_short v[26:27], v24, off
	s_mov_b64 exec, s[30:31]
	v_addc_co_u32_e64 v2, vcc, 0, v2, s[0:1]
	v_subb_co_u32_e64 v34, vcc, v34, 0, s[24:25]
	s_mov_b64 s[0:1], 0x108
	v_lshl_add_u64 v[24:25], v[30:31], 0, s[0:1]
	v_med3_i32 v35, v34, 0, 1
	v_sub_u32_e32 v35, v36, v35
	v_cmp_gt_i32_sdwa s[0:1], v20, v35 src0_sel:WORD_0 src1_sel:DWORD
	v_cmp_eq_u32_sdwa s[24:25], v20, v36 src0_sel:WORD_0 src1_sel:DWORD
	v_lshl_add_u64 v[26:27], v[2:3], 1, v[38:39]
	s_and_saveexec_b64 s[30:31], s[0:1]
	global_store_short v[26:27], v24, off
	s_mov_b64 exec, s[30:31]
	v_addc_co_u32_e64 v2, vcc, 0, v2, s[0:1]
	v_subb_co_u32_e64 v34, vcc, v34, 0, s[24:25]
	s_mov_b64 s[0:1], 0x109
	v_lshl_add_u64 v[24:25], v[30:31], 0, s[0:1]
	v_med3_i32 v35, v34, 0, 1
	v_sub_u32_e32 v35, v36, v35
	v_cmp_gt_i32_sdwa s[0:1], v20, v35 src0_sel:WORD_1 src1_sel:DWORD
	v_cmp_eq_u32_sdwa s[24:25], v20, v36 src0_sel:WORD_1 src1_sel:DWORD
	v_lshl_add_u64 v[26:27], v[2:3], 1, v[38:39]
	s_and_saveexec_b64 s[30:31], s[0:1]
	global_store_short v[26:27], v24, off
	s_mov_b64 exec, s[30:31]
	v_addc_co_u32_e64 v2, vcc, 0, v2, s[0:1]
	v_subb_co_u32_e64 v34, vcc, v34, 0, s[24:25]
	s_mov_b64 s[0:1], 0x10a
	v_lshl_add_u64 v[24:25], v[30:31], 0, s[0:1]
	v_med3_i32 v35, v34, 0, 1
	v_sub_u32_e32 v35, v36, v35
	v_cmp_gt_i32_sdwa s[0:1], v21, v35 src0_sel:WORD_0 src1_sel:DWORD
	v_cmp_eq_u32_sdwa s[24:25], v21, v36 src0_sel:WORD_0 src1_sel:DWORD
	v_lshl_add_u64 v[26:27], v[2:3], 1, v[38:39]
	s_and_saveexec_b64 s[30:31], s[0:1]
	global_store_short v[26:27], v24, off
	s_mov_b64 exec, s[30:31]
	v_addc_co_u32_e64 v2, vcc, 0, v2, s[0:1]
	v_subb_co_u32_e64 v34, vcc, v34, 0, s[24:25]
	s_mov_b64 s[0:1], 0x10b
	v_lshl_add_u64 v[24:25], v[30:31], 0, s[0:1]
	v_med3_i32 v35, v34, 0, 1
	v_sub_u32_e32 v35, v36, v35
	v_cmp_gt_i32_sdwa s[0:1], v21, v35 src0_sel:WORD_1 src1_sel:DWORD
	v_cmp_eq_u32_sdwa s[24:25], v21, v36 src0_sel:WORD_1 src1_sel:DWORD
	v_lshl_add_u64 v[20:21], v[2:3], 1, v[38:39]
	s_and_saveexec_b64 s[30:31], s[0:1]
	global_store_short v[20:21], v24, off
	s_mov_b64 exec, s[30:31]
	v_addc_co_u32_e64 v2, vcc, 0, v2, s[0:1]
	v_subb_co_u32_e64 v34, vcc, v34, 0, s[24:25]
	s_mov_b64 s[0:1], 0x10c
	v_lshl_add_u64 v[20:21], v[30:31], 0, s[0:1]
	v_med3_i32 v35, v34, 0, 1
	v_sub_u32_e32 v35, v36, v35
	v_cmp_gt_i32_sdwa s[0:1], v22, v35 src0_sel:WORD_0 src1_sel:DWORD
	v_cmp_eq_u32_sdwa s[24:25], v22, v36 src0_sel:WORD_0 src1_sel:DWORD
	v_lshl_add_u64 v[24:25], v[2:3], 1, v[38:39]
	s_and_saveexec_b64 s[30:31], s[0:1]
	global_store_short v[24:25], v20, off
	s_mov_b64 exec, s[30:31]
	v_addc_co_u32_e64 v2, vcc, 0, v2, s[0:1]
	v_subb_co_u32_e64 v34, vcc, v34, 0, s[24:25]
	s_mov_b64 s[0:1], 0x10d
	v_lshl_add_u64 v[20:21], v[30:31], 0, s[0:1]
	v_med3_i32 v35, v34, 0, 1
	v_sub_u32_e32 v35, v36, v35
	v_cmp_gt_i32_sdwa s[0:1], v22, v35 src0_sel:WORD_1 src1_sel:DWORD
	v_cmp_eq_u32_sdwa s[24:25], v22, v36 src0_sel:WORD_1 src1_sel:DWORD
	v_lshl_add_u64 v[24:25], v[2:3], 1, v[38:39]
	s_and_saveexec_b64 s[30:31], s[0:1]
	global_store_short v[24:25], v20, off
	s_mov_b64 exec, s[30:31]
	v_addc_co_u32_e64 v2, vcc, 0, v2, s[0:1]
	v_subb_co_u32_e64 v34, vcc, v34, 0, s[24:25]
	s_mov_b64 s[0:1], 0x10e
	v_lshl_add_u64 v[20:21], v[30:31], 0, s[0:1]
	v_med3_i32 v35, v34, 0, 1
	v_sub_u32_e32 v35, v36, v35
	v_cmp_gt_i32_sdwa s[0:1], v23, v35 src0_sel:WORD_0 src1_sel:DWORD
	v_cmp_eq_u32_sdwa s[24:25], v23, v36 src0_sel:WORD_0 src1_sel:DWORD
	v_lshl_add_u64 v[24:25], v[2:3], 1, v[38:39]
	s_and_saveexec_b64 s[30:31], s[0:1]
	global_store_short v[24:25], v20, off
	s_mov_b64 exec, s[30:31]
	v_addc_co_u32_e64 v2, vcc, 0, v2, s[0:1]
	v_subb_co_u32_e64 v34, vcc, v34, 0, s[24:25]
	v_sub_u32_e32 v34, v37, v34
	v_min_i32_e32 v35, v34, v37
	v_sub_u32_e32 v35, v2, v35
	v_cmp_le_u32_sdwa s[24:25], v23, v36 src0_sel:WORD_1 src1_sel:DWORD
	s_mov_b64 s[0:1], 0
	s_and_saveexec_b64 s[30:31], s[24:25]
	s_xor_b64 s[24:25], exec, s[30:31]
	s_cbranch_execz .LBB0_1232
	v_cmp_eq_u32_sdwa s[0:1], v23, v36 src0_sel:WORD_1 src1_sel:DWORD
	v_cmp_lt_i32_e32 vcc, v34, v37
	s_and_b64 s[34:35], s[0:1], vcc
	s_mov_b64 s[0:1], 0
	s_and_saveexec_b64 s[30:31], s[34:35]
	v_add_u32_e32 v2, v34, v35
	s_mov_b64 s[0:1], exec
	v_mov_b64_e32 v[20:21], v[2:3]
	s_or_b64 exec, exec, s[30:31]
	s_and_b64 s[0:1], s[0:1], exec
	s_andn2_saveexec_b64 s[24:25], s[24:25]
	s_cbranch_execnz .LBB0_1233

.LBB0_976:
	ds_read_u16 v2, v50 offset:36928
	s_waitcnt lgkmcnt(0)
	v_cmp_ne_u16_e32 vcc, 0, v2
	s_and_saveexec_b64 s[18:19], vcc
	s_cbranch_execz .LBB0_1103
	ds_read_u16 v2, v49 offset:36928
	s_waitcnt vmcnt(5)
	v_add_u32_e32 v20, 0x11240, v49
	ds_read_b32 v20, v20
	v_lshl_add_u64 v[22:23], v[40:41], 0, s[16:17]
	s_mov_b64 s[0:1], 0x200
	s_waitcnt lgkmcnt(1)
	v_lshrrev_b32_e32 v21, 8, v2
	v_and_b32_e32 v2, 0xff, v2
	v_cndmask_b32_e64 v21, v21, 0, s[22:23]
	v_cndmask_b32_e64 v2, v2, 0, s[22:23]
	s_waitcnt vmcnt(4) lgkmcnt(0)
	v_add_u32_sdwa v26, v21, v20 dst_sel:DWORD dst_unused:UNUSED_PAD src0_sel:DWORD src1_sel:WORD_1
	v_add_u32_sdwa v27, v2, v20 dst_sel:DWORD dst_unused:UNUSED_PAD src0_sel:DWORD src1_sel:WORD_0
	v_lshl_add_u64 v[20:21], v[22:23], 0, s[0:1]
	s_waitcnt vmcnt(2)
	v_min_i32_e32 v2, v26, v37
	v_add_u32_e32 v2, v2, v27
	v_sub_u32_e32 v26, v37, v26
	v_med3_i32 v27, v26, 0, 1
	v_sub_u32_e32 v27, v36, v27
	v_cmp_gt_i32_sdwa s[0:1], v16, v27 src0_sel:WORD_0 src1_sel:DWORD
	v_cmp_eq_u32_sdwa s[24:25], v16, v36 src0_sel:WORD_0 src1_sel:DWORD
	v_lshl_add_u64 v[24:25], v[2:3], 1, v[38:39]
	s_and_saveexec_b64 s[28:29], s[0:1]
	global_store_short v[24:25], v20, off
	s_mov_b64 exec, s[28:29]
	v_addc_co_u32_e64 v2, vcc, 0, v2, s[0:1]
	v_subb_co_u32_e64 v26, vcc, v26, 0, s[24:25]
	s_mov_b64 s[0:1], 0x201
	v_lshl_add_u64 v[24:25], v[22:23], 0, s[0:1]
	v_med3_i32 v27, v26, 0, 1
	v_sub_u32_e32 v27, v36, v27
	v_cmp_gt_i32_sdwa s[0:1], v16, v27 src0_sel:WORD_1 src1_sel:DWORD
	v_cmp_eq_u32_sdwa s[24:25], v16, v36 src0_sel:WORD_1 src1_sel:DWORD
	v_lshl_add_u64 v[28:29], v[2:3], 1, v[38:39]
	s_and_saveexec_b64 s[28:29], s[0:1]
	global_store_short v[28:29], v24, off
	s_mov_b64 exec, s[28:29]
	v_addc_co_u32_e64 v2, vcc, 0, v2, s[0:1]
	v_subb_co_u32_e64 v26, vcc, v26, 0, s[24:25]
	s_mov_b64 s[0:1], 0x202
	v_lshl_add_u64 v[24:25], v[22:23], 0, s[0:1]
	v_med3_i32 v27, v26, 0, 1
	v_sub_u32_e32 v27, v36, v27
	v_cmp_gt_i32_sdwa s[0:1], v17, v27 src0_sel:WORD_0 src1_sel:DWORD
	v_cmp_eq_u32_sdwa s[24:25], v17, v36 src0_sel:WORD_0 src1_sel:DWORD
	v_lshl_add_u64 v[28:29], v[2:3], 1, v[38:39]
	s_and_saveexec_b64 s[28:29], s[0:1]
	global_store_short v[28:29], v24, off
	s_mov_b64 exec, s[28:29]
	v_addc_co_u32_e64 v2, vcc, 0, v2, s[0:1]
	v_subb_co_u32_e64 v26, vcc, v26, 0, s[24:25]
	s_mov_b64 s[0:1], 0x203
	v_lshl_add_u64 v[24:25], v[22:23], 0, s[0:1]
	v_med3_i32 v27, v26, 0, 1
	v_sub_u32_e32 v27, v36, v27
	v_cmp_gt_i32_sdwa s[0:1], v17, v27 src0_sel:WORD_1 src1_sel:DWORD
	v_cmp_eq_u32_sdwa s[24:25], v17, v36 src0_sel:WORD_1 src1_sel:DWORD
	v_lshl_add_u64 v[16:17], v[2:3], 1, v[38:39]
	s_and_saveexec_b64 s[28:29], s[0:1]
	global_store_short v[16:17], v24, off
	s_mov_b64 exec, s[28:29]
	v_addc_co_u32_e64 v2, vcc, 0, v2, s[0:1]
	v_subb_co_u32_e64 v26, vcc, v26, 0, s[24:25]
	s_mov_b64 s[0:1], 0x204
	v_lshl_add_u64 v[16:17], v[22:23], 0, s[0:1]
	v_med3_i32 v27, v26, 0, 1
	v_sub_u32_e32 v27, v36, v27
	v_cmp_gt_i32_sdwa s[0:1], v18, v27 src0_sel:WORD_0 src1_sel:DWORD
	v_cmp_eq_u32_sdwa s[24:25], v18, v36 src0_sel:WORD_0 src1_sel:DWORD
	v_lshl_add_u64 v[24:25], v[2:3], 1, v[38:39]
	s_and_saveexec_b64 s[28:29], s[0:1]
	global_store_short v[24:25], v16, off
	s_mov_b64 exec, s[28:29]
	v_addc_co_u32_e64 v2, vcc, 0, v2, s[0:1]
	v_subb_co_u32_e64 v26, vcc, v26, 0, s[24:25]
	s_mov_b64 s[0:1], 0x205
	v_lshl_add_u64 v[16:17], v[22:23], 0, s[0:1]
	v_med3_i32 v27, v26, 0, 1
	v_sub_u32_e32 v27, v36, v27
	v_cmp_gt_i32_sdwa s[0:1], v18, v27 src0_sel:WORD_1 src1_sel:DWORD
	v_cmp_eq_u32_sdwa s[24:25], v18, v36 src0_sel:WORD_1 src1_sel:DWORD
	v_lshl_add_u64 v[24:25], v[2:3], 1, v[38:39]
	s_and_saveexec_b64 s[28:29], s[0:1]
	global_store_short v[24:25], v16, off
	s_mov_b64 exec, s[28:29]
	v_addc_co_u32_e64 v2, vcc, 0, v2, s[0:1]
	v_subb_co_u32_e64 v26, vcc, v26, 0, s[24:25]
	s_mov_b64 s[0:1], 0x206
	v_lshl_add_u64 v[16:17], v[22:23], 0, s[0:1]
	v_med3_i32 v27, v26, 0, 1
	v_sub_u32_e32 v27, v36, v27
	v_cmp_gt_i32_sdwa s[0:1], v19, v27 src0_sel:WORD_0 src1_sel:DWORD
	v_cmp_eq_u32_sdwa s[24:25], v19, v36 src0_sel:WORD_0 src1_sel:DWORD
	v_lshl_add_u64 v[24:25], v[2:3], 1, v[38:39]
	s_and_saveexec_b64 s[28:29], s[0:1]
	global_store_short v[24:25], v16, off
	s_mov_b64 exec, s[28:29]
	v_addc_co_u32_e64 v2, vcc, 0, v2, s[0:1]
	v_subb_co_u32_e64 v26, vcc, v26, 0, s[24:25]
	s_mov_b64 s[0:1], 0x207
	v_lshl_add_u64 v[16:17], v[22:23], 0, s[0:1]
	v_med3_i32 v27, v26, 0, 1
	v_sub_u32_e32 v27, v36, v27
	v_cmp_gt_i32_sdwa s[0:1], v19, v27 src0_sel:WORD_1 src1_sel:DWORD
	v_cmp_eq_u32_sdwa s[24:25], v19, v36 src0_sel:WORD_1 src1_sel:DWORD
	v_lshl_add_u64 v[18:19], v[2:3], 1, v[38:39]
	s_and_saveexec_b64 s[28:29], s[0:1]
	global_store_short v[18:19], v16, off
	s_mov_b64 exec, s[28:29]
	v_addc_co_u32_e64 v2, vcc, 0, v2, s[0:1]
	v_subb_co_u32_e64 v26, vcc, v26, 0, s[24:25]
	s_mov_b64 s[0:1], 0x208
	v_lshl_add_u64 v[16:17], v[22:23], 0, s[0:1]
	v_med3_i32 v27, v26, 0, 1
	v_sub_u32_e32 v27, v36, v27
	v_cmp_gt_i32_sdwa s[0:1], v12, v27 src0_sel:WORD_0 src1_sel:DWORD
	v_cmp_eq_u32_sdwa s[24:25], v12, v36 src0_sel:WORD_0 src1_sel:DWORD
	v_lshl_add_u64 v[18:19], v[2:3], 1, v[38:39]
	s_and_saveexec_b64 s[28:29], s[0:1]
	global_store_short v[18:19], v16, off
	s_mov_b64 exec, s[28:29]
	v_addc_co_u32_e64 v2, vcc, 0, v2, s[0:1]
	v_subb_co_u32_e64 v26, vcc, v26, 0, s[24:25]
	s_mov_b64 s[0:1], 0x209
	v_lshl_add_u64 v[16:17], v[22:23], 0, s[0:1]
	v_med3_i32 v27, v26, 0, 1
	v_sub_u32_e32 v27, v36, v27
	v_cmp_gt_i32_sdwa s[0:1], v12, v27 src0_sel:WORD_1 src1_sel:DWORD
	v_cmp_eq_u32_sdwa s[24:25], v12, v36 src0_sel:WORD_1 src1_sel:DWORD
	v_lshl_add_u64 v[18:19], v[2:3], 1, v[38:39]
	s_and_saveexec_b64 s[28:29], s[0:1]
	global_store_short v[18:19], v16, off
	s_mov_b64 exec, s[28:29]
	v_addc_co_u32_e64 v2, vcc, 0, v2, s[0:1]
	v_subb_co_u32_e64 v26, vcc, v26, 0, s[24:25]
	s_mov_b64 s[0:1], 0x20a
	v_lshl_add_u64 v[16:17], v[22:23], 0, s[0:1]
	v_med3_i32 v27, v26, 0, 1
	v_sub_u32_e32 v27, v36, v27
	v_cmp_gt_i32_sdwa s[0:1], v13, v27 src0_sel:WORD_0 src1_sel:DWORD
	v_cmp_eq_u32_sdwa s[24:25], v13, v36 src0_sel:WORD_0 src1_sel:DWORD
	v_lshl_add_u64 v[18:19], v[2:3], 1, v[38:39]
	s_and_saveexec_b64 s[28:29], s[0:1]
	global_store_short v[18:19], v16, off
	s_mov_b64 exec, s[28:29]
	v_addc_co_u32_e64 v2, vcc, 0, v2, s[0:1]
	v_subb_co_u32_e64 v26, vcc, v26, 0, s[24:25]
	s_mov_b64 s[0:1], 0x20b
	v_lshl_add_u64 v[16:17], v[22:23], 0, s[0:1]
	v_med3_i32 v27, v26, 0, 1
	v_sub_u32_e32 v27, v36, v27
	v_cmp_gt_i32_sdwa s[0:1], v13, v27 src0_sel:WORD_1 src1_sel:DWORD
	v_cmp_eq_u32_sdwa s[24:25], v13, v36 src0_sel:WORD_1 src1_sel:DWORD
	v_lshl_add_u64 v[12:13], v[2:3], 1, v[38:39]
	s_and_saveexec_b64 s[28:29], s[0:1]
	global_store_short v[12:13], v16, off
	s_mov_b64 exec, s[28:29]
	v_addc_co_u32_e64 v2, vcc, 0, v2, s[0:1]
	v_subb_co_u32_e64 v26, vcc, v26, 0, s[24:25]
	s_mov_b64 s[0:1], 0x20c
	v_lshl_add_u64 v[12:13], v[22:23], 0, s[0:1]
	v_med3_i32 v27, v26, 0, 1
	v_sub_u32_e32 v27, v36, v27
	v_cmp_gt_i32_sdwa s[0:1], v14, v27 src0_sel:WORD_0 src1_sel:DWORD
	v_cmp_eq_u32_sdwa s[24:25], v14, v36 src0_sel:WORD_0 src1_sel:DWORD
	v_lshl_add_u64 v[16:17], v[2:3], 1, v[38:39]
	s_and_saveexec_b64 s[28:29], s[0:1]
	global_store_short v[16:17], v12, off
	s_mov_b64 exec, s[28:29]
	v_addc_co_u32_e64 v2, vcc, 0, v2, s[0:1]
	v_subb_co_u32_e64 v26, vcc, v26, 0, s[24:25]
	s_mov_b64 s[0:1], 0x20d
	v_lshl_add_u64 v[12:13], v[22:23], 0, s[0:1]
	v_med3_i32 v27, v26, 0, 1
	v_sub_u32_e32 v27, v36, v27
	v_cmp_gt_i32_sdwa s[0:1], v14, v27 src0_sel:WORD_1 src1_sel:DWORD
	v_cmp_eq_u32_sdwa s[24:25], v14, v36 src0_sel:WORD_1 src1_sel:DWORD
	v_lshl_add_u64 v[16:17], v[2:3], 1, v[38:39]
	s_and_saveexec_b64 s[28:29], s[0:1]
	global_store_short v[16:17], v12, off
	s_mov_b64 exec, s[28:29]
	v_addc_co_u32_e64 v2, vcc, 0, v2, s[0:1]
	v_subb_co_u32_e64 v26, vcc, v26, 0, s[24:25]
	s_mov_b64 s[0:1], 0x20e
	v_lshl_add_u64 v[12:13], v[22:23], 0, s[0:1]
	v_med3_i32 v27, v26, 0, 1
	v_sub_u32_e32 v27, v36, v27
	v_cmp_gt_i32_sdwa s[0:1], v15, v27 src0_sel:WORD_0 src1_sel:DWORD
	v_cmp_eq_u32_sdwa s[24:25], v15, v36 src0_sel:WORD_0 src1_sel:DWORD
	v_lshl_add_u64 v[16:17], v[2:3], 1, v[38:39]
	s_and_saveexec_b64 s[28:29], s[0:1]
	global_store_short v[16:17], v12, off
	s_mov_b64 exec, s[28:29]
	v_addc_co_u32_e64 v2, vcc, 0, v2, s[0:1]
	v_subb_co_u32_e64 v26, vcc, v26, 0, s[24:25]
	v_sub_u32_e32 v26, v37, v26
	v_min_i32_e32 v27, v26, v37
	v_sub_u32_e32 v27, v2, v27
	v_cmp_le_u32_sdwa s[24:25], v15, v36 src0_sel:WORD_1 src1_sel:DWORD
	s_mov_b64 s[0:1], 0
	s_and_saveexec_b64 s[28:29], s[24:25]
	s_xor_b64 s[24:25], exec, s[28:29]
	s_cbranch_execz .LBB0_1234
	v_cmp_eq_u32_sdwa s[0:1], v15, v36 src0_sel:WORD_1 src1_sel:DWORD
	v_cmp_lt_i32_e32 vcc, v26, v37
	s_and_b64 s[30:31], s[0:1], vcc
	s_mov_b64 s[0:1], 0
	s_and_saveexec_b64 s[28:29], s[30:31]
	v_add_u32_e32 v2, v26, v27
	s_mov_b64 s[0:1], exec
	v_mov_b64_e32 v[12:13], v[2:3]
	s_or_b64 exec, exec, s[28:29]
	s_and_b64 s[0:1], s[0:1], exec
	s_andn2_saveexec_b64 s[24:25], s[24:25]
	s_cbranch_execnz .LBB0_1235

.LBB0_1104:
	ds_read_u16 v2, v50 offset:36960
	s_waitcnt lgkmcnt(0)
	v_cmp_ne_u16_e32 vcc, 0, v2
	s_and_saveexec_b64 s[18:19], vcc
	s_cbranch_execz .LBB0_710
	ds_read_u16 v2, v49 offset:36960
	s_waitcnt vmcnt(3)
	v_add_u32_e32 v12, 0x11260, v49
	ds_read_b32 v12, v12
	v_lshl_add_u64 v[14:15], v[40:41], 0, s[16:17]
	s_mov_b64 s[0:1], 0x300
	s_waitcnt lgkmcnt(1)
	v_lshrrev_b32_e32 v13, 8, v2
	v_and_b32_e32 v2, 0xff, v2
	v_cndmask_b32_e64 v13, v13, 0, s[22:23]
	v_cndmask_b32_e64 v2, v2, 0, s[22:23]
	s_waitcnt vmcnt(2) lgkmcnt(0)
	v_add_u32_sdwa v18, v13, v12 dst_sel:DWORD dst_unused:UNUSED_PAD src0_sel:DWORD src1_sel:WORD_1
	v_add_u32_sdwa v19, v2, v12 dst_sel:DWORD dst_unused:UNUSED_PAD src0_sel:DWORD src1_sel:WORD_0
	v_lshl_add_u64 v[12:13], v[14:15], 0, s[0:1]
	s_waitcnt vmcnt(0)
	v_min_i32_e32 v2, v18, v37
	v_add_u32_e32 v2, v2, v19
	v_sub_u32_e32 v18, v37, v18
	v_med3_i32 v19, v18, 0, 1
	v_sub_u32_e32 v19, v36, v19
	v_cmp_gt_i32_sdwa s[0:1], v8, v19 src0_sel:WORD_0 src1_sel:DWORD
	v_cmp_eq_u32_sdwa s[24:25], v8, v36 src0_sel:WORD_0 src1_sel:DWORD
	v_lshl_add_u64 v[16:17], v[2:3], 1, v[38:39]
	s_and_saveexec_b64 s[26:27], s[0:1]
	global_store_short v[16:17], v12, off
	s_mov_b64 exec, s[26:27]
	v_addc_co_u32_e64 v2, vcc, 0, v2, s[0:1]
	v_subb_co_u32_e64 v18, vcc, v18, 0, s[24:25]
	s_mov_b64 s[0:1], 0x301
	v_lshl_add_u64 v[16:17], v[14:15], 0, s[0:1]
	v_med3_i32 v19, v18, 0, 1
	v_sub_u32_e32 v19, v36, v19
	v_cmp_gt_i32_sdwa s[0:1], v8, v19 src0_sel:WORD_1 src1_sel:DWORD
	v_cmp_eq_u32_sdwa s[24:25], v8, v36 src0_sel:WORD_1 src1_sel:DWORD
	v_lshl_add_u64 v[20:21], v[2:3], 1, v[38:39]
	s_and_saveexec_b64 s[26:27], s[0:1]
	global_store_short v[20:21], v16, off
	s_mov_b64 exec, s[26:27]
	v_addc_co_u32_e64 v2, vcc, 0, v2, s[0:1]
	v_subb_co_u32_e64 v18, vcc, v18, 0, s[24:25]
	s_mov_b64 s[0:1], 0x302
	v_lshl_add_u64 v[16:17], v[14:15], 0, s[0:1]
	v_med3_i32 v19, v18, 0, 1
	v_sub_u32_e32 v19, v36, v19
	v_cmp_gt_i32_sdwa s[0:1], v9, v19 src0_sel:WORD_0 src1_sel:DWORD
	v_cmp_eq_u32_sdwa s[24:25], v9, v36 src0_sel:WORD_0 src1_sel:DWORD
	v_lshl_add_u64 v[20:21], v[2:3], 1, v[38:39]
	s_and_saveexec_b64 s[26:27], s[0:1]
	global_store_short v[20:21], v16, off
	s_mov_b64 exec, s[26:27]
	v_addc_co_u32_e64 v2, vcc, 0, v2, s[0:1]
	v_subb_co_u32_e64 v18, vcc, v18, 0, s[24:25]
	s_mov_b64 s[0:1], 0x303
	v_lshl_add_u64 v[16:17], v[14:15], 0, s[0:1]
	v_med3_i32 v19, v18, 0, 1
	v_sub_u32_e32 v19, v36, v19
	v_cmp_gt_i32_sdwa s[0:1], v9, v19 src0_sel:WORD_1 src1_sel:DWORD
	v_cmp_eq_u32_sdwa s[24:25], v9, v36 src0_sel:WORD_1 src1_sel:DWORD
	v_lshl_add_u64 v[8:9], v[2:3], 1, v[38:39]
	s_and_saveexec_b64 s[26:27], s[0:1]
	global_store_short v[8:9], v16, off
	s_mov_b64 exec, s[26:27]
	v_addc_co_u32_e64 v2, vcc, 0, v2, s[0:1]
	v_subb_co_u32_e64 v18, vcc, v18, 0, s[24:25]
	s_mov_b64 s[0:1], 0x304
	v_lshl_add_u64 v[8:9], v[14:15], 0, s[0:1]
	v_med3_i32 v19, v18, 0, 1
	v_sub_u32_e32 v19, v36, v19
	v_cmp_gt_i32_sdwa s[0:1], v10, v19 src0_sel:WORD_0 src1_sel:DWORD
	v_cmp_eq_u32_sdwa s[24:25], v10, v36 src0_sel:WORD_0 src1_sel:DWORD
	v_lshl_add_u64 v[16:17], v[2:3], 1, v[38:39]
	s_and_saveexec_b64 s[26:27], s[0:1]
	global_store_short v[16:17], v8, off
	s_mov_b64 exec, s[26:27]
	v_addc_co_u32_e64 v2, vcc, 0, v2, s[0:1]
	v_subb_co_u32_e64 v18, vcc, v18, 0, s[24:25]
	s_mov_b64 s[0:1], 0x305
	v_lshl_add_u64 v[8:9], v[14:15], 0, s[0:1]
	v_med3_i32 v19, v18, 0, 1
	v_sub_u32_e32 v19, v36, v19
	v_cmp_gt_i32_sdwa s[0:1], v10, v19 src0_sel:WORD_1 src1_sel:DWORD
	v_cmp_eq_u32_sdwa s[24:25], v10, v36 src0_sel:WORD_1 src1_sel:DWORD
	v_lshl_add_u64 v[16:17], v[2:3], 1, v[38:39]
	s_and_saveexec_b64 s[26:27], s[0:1]
	global_store_short v[16:17], v8, off
	s_mov_b64 exec, s[26:27]
	v_addc_co_u32_e64 v2, vcc, 0, v2, s[0:1]
	v_subb_co_u32_e64 v18, vcc, v18, 0, s[24:25]
	s_mov_b64 s[0:1], 0x306
	v_lshl_add_u64 v[8:9], v[14:15], 0, s[0:1]
	v_med3_i32 v19, v18, 0, 1
	v_sub_u32_e32 v19, v36, v19
	v_cmp_gt_i32_sdwa s[0:1], v11, v19 src0_sel:WORD_0 src1_sel:DWORD
	v_cmp_eq_u32_sdwa s[24:25], v11, v36 src0_sel:WORD_0 src1_sel:DWORD
	v_lshl_add_u64 v[16:17], v[2:3], 1, v[38:39]
	s_and_saveexec_b64 s[26:27], s[0:1]
	global_store_short v[16:17], v8, off
	s_mov_b64 exec, s[26:27]
	v_addc_co_u32_e64 v2, vcc, 0, v2, s[0:1]
	v_subb_co_u32_e64 v18, vcc, v18, 0, s[24:25]
	s_mov_b64 s[0:1], 0x307
	v_lshl_add_u64 v[8:9], v[14:15], 0, s[0:1]
	v_med3_i32 v19, v18, 0, 1
	v_sub_u32_e32 v19, v36, v19
	v_cmp_gt_i32_sdwa s[0:1], v11, v19 src0_sel:WORD_1 src1_sel:DWORD
	v_cmp_eq_u32_sdwa s[24:25], v11, v36 src0_sel:WORD_1 src1_sel:DWORD
	v_lshl_add_u64 v[10:11], v[2:3], 1, v[38:39]
	s_and_saveexec_b64 s[26:27], s[0:1]
	global_store_short v[10:11], v8, off
	s_mov_b64 exec, s[26:27]
	v_addc_co_u32_e64 v2, vcc, 0, v2, s[0:1]
	v_subb_co_u32_e64 v18, vcc, v18, 0, s[24:25]
	s_mov_b64 s[0:1], 0x308
	v_lshl_add_u64 v[8:9], v[14:15], 0, s[0:1]
	v_med3_i32 v19, v18, 0, 1
	v_sub_u32_e32 v19, v36, v19
	v_cmp_gt_i32_sdwa s[0:1], v4, v19 src0_sel:WORD_0 src1_sel:DWORD
	v_cmp_eq_u32_sdwa s[24:25], v4, v36 src0_sel:WORD_0 src1_sel:DWORD
	v_lshl_add_u64 v[10:11], v[2:3], 1, v[38:39]
	s_and_saveexec_b64 s[26:27], s[0:1]
	global_store_short v[10:11], v8, off
	s_mov_b64 exec, s[26:27]
	v_addc_co_u32_e64 v2, vcc, 0, v2, s[0:1]
	v_subb_co_u32_e64 v18, vcc, v18, 0, s[24:25]
	s_mov_b64 s[0:1], 0x309
	v_lshl_add_u64 v[8:9], v[14:15], 0, s[0:1]
	v_med3_i32 v19, v18, 0, 1
	v_sub_u32_e32 v19, v36, v19
	v_cmp_gt_i32_sdwa s[0:1], v4, v19 src0_sel:WORD_1 src1_sel:DWORD
	v_cmp_eq_u32_sdwa s[24:25], v4, v36 src0_sel:WORD_1 src1_sel:DWORD
	v_lshl_add_u64 v[10:11], v[2:3], 1, v[38:39]
	s_and_saveexec_b64 s[26:27], s[0:1]
	global_store_short v[10:11], v8, off
	s_mov_b64 exec, s[26:27]
	v_addc_co_u32_e64 v2, vcc, 0, v2, s[0:1]
	v_subb_co_u32_e64 v18, vcc, v18, 0, s[24:25]
	s_mov_b64 s[0:1], 0x30a
	v_lshl_add_u64 v[8:9], v[14:15], 0, s[0:1]
	v_med3_i32 v19, v18, 0, 1
	v_sub_u32_e32 v19, v36, v19
	v_cmp_gt_i32_sdwa s[0:1], v5, v19 src0_sel:WORD_0 src1_sel:DWORD
	v_cmp_eq_u32_sdwa s[24:25], v5, v36 src0_sel:WORD_0 src1_sel:DWORD
	v_lshl_add_u64 v[10:11], v[2:3], 1, v[38:39]
	s_and_saveexec_b64 s[26:27], s[0:1]
	global_store_short v[10:11], v8, off
	s_mov_b64 exec, s[26:27]
	v_addc_co_u32_e64 v2, vcc, 0, v2, s[0:1]
	v_subb_co_u32_e64 v18, vcc, v18, 0, s[24:25]
	s_mov_b64 s[0:1], 0x30b
	v_lshl_add_u64 v[8:9], v[14:15], 0, s[0:1]
	v_med3_i32 v19, v18, 0, 1
	v_sub_u32_e32 v19, v36, v19
	v_cmp_gt_i32_sdwa s[0:1], v5, v19 src0_sel:WORD_1 src1_sel:DWORD
	v_cmp_eq_u32_sdwa s[24:25], v5, v36 src0_sel:WORD_1 src1_sel:DWORD
	v_lshl_add_u64 v[4:5], v[2:3], 1, v[38:39]
	s_and_saveexec_b64 s[26:27], s[0:1]
	global_store_short v[4:5], v8, off
	s_mov_b64 exec, s[26:27]
	v_addc_co_u32_e64 v2, vcc, 0, v2, s[0:1]
	v_subb_co_u32_e64 v18, vcc, v18, 0, s[24:25]
	s_mov_b64 s[0:1], 0x30c
	v_lshl_add_u64 v[4:5], v[14:15], 0, s[0:1]
	v_med3_i32 v19, v18, 0, 1
	v_sub_u32_e32 v19, v36, v19
	v_cmp_gt_i32_sdwa s[0:1], v6, v19 src0_sel:WORD_0 src1_sel:DWORD
	v_cmp_eq_u32_sdwa s[24:25], v6, v36 src0_sel:WORD_0 src1_sel:DWORD
	v_lshl_add_u64 v[8:9], v[2:3], 1, v[38:39]
	s_and_saveexec_b64 s[26:27], s[0:1]
	global_store_short v[8:9], v4, off
	s_mov_b64 exec, s[26:27]
	v_addc_co_u32_e64 v2, vcc, 0, v2, s[0:1]
	v_subb_co_u32_e64 v18, vcc, v18, 0, s[24:25]
	s_mov_b64 s[0:1], 0x30d
	v_lshl_add_u64 v[4:5], v[14:15], 0, s[0:1]
	v_med3_i32 v19, v18, 0, 1
	v_sub_u32_e32 v19, v36, v19
	v_cmp_gt_i32_sdwa s[0:1], v6, v19 src0_sel:WORD_1 src1_sel:DWORD
	v_cmp_eq_u32_sdwa s[24:25], v6, v36 src0_sel:WORD_1 src1_sel:DWORD
	v_lshl_add_u64 v[8:9], v[2:3], 1, v[38:39]
	s_and_saveexec_b64 s[26:27], s[0:1]
	global_store_short v[8:9], v4, off
	s_mov_b64 exec, s[26:27]
	v_addc_co_u32_e64 v2, vcc, 0, v2, s[0:1]
	v_subb_co_u32_e64 v18, vcc, v18, 0, s[24:25]
	s_mov_b64 s[0:1], 0x30e
	v_lshl_add_u64 v[4:5], v[14:15], 0, s[0:1]
	v_med3_i32 v19, v18, 0, 1
	v_sub_u32_e32 v19, v36, v19
	v_cmp_gt_i32_sdwa s[0:1], v7, v19 src0_sel:WORD_0 src1_sel:DWORD
	v_cmp_eq_u32_sdwa s[24:25], v7, v36 src0_sel:WORD_0 src1_sel:DWORD
	v_lshl_add_u64 v[8:9], v[2:3], 1, v[38:39]
	s_and_saveexec_b64 s[26:27], s[0:1]
	global_store_short v[8:9], v4, off
	s_mov_b64 exec, s[26:27]
	v_addc_co_u32_e64 v2, vcc, 0, v2, s[0:1]
	v_subb_co_u32_e64 v18, vcc, v18, 0, s[24:25]
	v_sub_u32_e32 v18, v37, v18
	v_min_i32_e32 v19, v18, v37
	v_sub_u32_e32 v19, v2, v19
	v_cmp_le_u32_sdwa s[24:25], v7, v36 src0_sel:WORD_1 src1_sel:DWORD
	s_mov_b64 s[0:1], 0
	s_and_saveexec_b64 s[26:27], s[24:25]
	s_xor_b64 s[24:25], exec, s[26:27]
	s_cbranch_execz .LBB0_1236
	v_cmp_eq_u32_sdwa s[0:1], v7, v36 src0_sel:WORD_1 src1_sel:DWORD
	v_cmp_lt_i32_e32 vcc, v18, v37
	s_and_b64 s[28:29], s[0:1], vcc
	s_mov_b64 s[0:1], 0
	s_and_saveexec_b64 s[26:27], s[28:29]
	v_add_u32_e32 v2, v18, v19
	s_mov_b64 s[0:1], exec
	v_mov_b64_e32 v[4:5], v[2:3]
	s_or_b64 exec, exec, s[26:27]
	s_and_b64 s[0:1], s[0:1], exec
	s_andn2_saveexec_b64 s[24:25], s[24:25]
	s_cbranch_execnz .LBB0_1237
